# v57 + stage-A work queue reordered: HBM-bound weight-transpose units dealt before the compute units (same units, different order)
# speedup vs baseline: 1.0045x; 1.0040x over previous
.LBB0_380:
	s_cmpk_lt_u32 s26, 0xa0
	s_cbranch_scc1 .Lqa_done
	v_readlane_b32 s100, v253, 29
	s_movk_i32 s101, 0x200
	s_cmp_eq_u32 s100, 3
	s_movk_i32 s100, 0x548
	s_cselect_b32 s100, s101, s100
	s_add_i32 s101, s100, 0xa0
	s_cmp_lt_u32 s26, s101
	s_cbranch_scc0 .Lqa_b
	s_add_i32 s26, s26, 0x300
	s_branch .Lqa_done
.Lqa_b:
	s_add_i32 s101, s101, 0x300
	s_cmp_lt_u32 s26, s101
	s_cbranch_scc0 .Lqa_done
	s_sub_i32 s26, s26, s100
